# P10 epilogue: bias vectors of the next unit fetched during the current epilogue into phase-dead VGPRs (no exposed round trip before the SwiGLU math)
# speedup vs baseline: 1.0042x; 1.0042x over previous
; #define PG8_GROWS(d0, d1, slot) do { _Pragma("unroll") for (int _i = 0; _i < 2; ++_i) { \
;         d0[_i] = (unsigned)g.rows[(slot) * 256 + gR[_i]] * (unsigned)(g.lda * 2) + gCb[_i]; d1[_i] = (unsigned)g.rows[(slot) * 256 + 128 + gR[_i]] * (unsigned)(g.lda * 2) + gCb[_i]; } } while (0)
; #define PG8_WAIT_V(n) asm volatile("s_waitcnt vmcnt(" #n ")" ::: "memory")
; #define PG8_BAR __builtin_amdgcn_s_barrier()
; template <class Epi, class Sched, bool ALIGN_EPI = false, bool SP2 = false, bool F8 = false, bool GATHER = false>
; __device__ __forceinline__ void gemm_phase(PG8_LAS unsigned char* lds, const Gemm g, const Sched& S, const Epi& E) {
;     ...
;     const char* cA = (const char*)g.A + (GATHER ? (size_t)0 : (size_t)cur.pm * tstepA); const char* cB = (const char*)g.Bt + (size_t)cur.pn * tstepB;
;     if constexpr (GATHER) { PG8_GROWS(gC0, gC1, 0); }
;     S.a_ready(cur);
;     if constexpr (SP2) {
;         PG8_STAGE(PG8_SB(0, 0), cB, voffB); PG8_STAGE(PG8_SB(0, 1), cB + hstepB, voffB); PG8_STAGE_A(PG8_SA(0, 0), cA, 0, false); PG8_STAGE_A(PG8_SA(0, 1), cA, 1, false);
;         if (wr == 1) PG8_BAR;
;         PG8_WAIT_V(2); PG8_BAR;
;         PG8_STAGE(PG8_SB(1, 0), cB + kstep, voffB); PG8_STAGE_A(PG8_SA(1, 0), cA + kstep, 0, false); PG8_STAGE(PG8_SB(1, 1), cB + hstepB + kstep, voffB);
;         PG8_WAIT_V(6); PG8_BAR;
;     } else {
;         PG8_STAGE(PG8_SB(0, 0), cB, voffB); PG8_STAGE_A(PG8_SA(0, 0), cA, 0, false); PG8_STAGE(PG8_SB(0, 1), cB + hstepB, voffB); PG8_STAGE_A(PG8_SA(0, 1), cA, 1, false);
;         if (wr == 1) PG8_BAR;
;         PG8_WAIT_V(4); PG8_BAR;
;         PG8_STAGE(PG8_SB(1, 0), cB + kstep, voffB); PG8_STAGE_A(PG8_SA(1, 0), cA + kstep, 0, false); PG8_STAGE(PG8_SB(1, 1), cB + hstepB + kstep, voffB);
;         PG8_WAIT_V(6); PG8_BAR;
;     }
;     __device__ __forceinline__ void operator()(const f32x4 (&acc)[2][2][4][2], const Unit& u, int wr, int wc, int fr, int fq) const {
;         const int e = u.pn >> 4, ct = u.pn & 15, row0 = u.pm * 256 + wr * 64 + fr, col = ct * 128 + wc * 32 + 8 * fq;
;         const float* bg = bgu + (size_t)e * 4096 + col; const f32x4 g0 = *(const f32x4*)bg, g1 = *(const f32x4*)(bg + 4);
;         const f32x4 u0 = (*(const f32x4*)(bg + 2048) + 1.0f) * F8_ASCALE, u1 = (*(const f32x4*)(bg + 2052) + 1.0f) * F8_ASCALE;
.LBB0_1403:
	s_or_b64 exec, exec, s[18:19]
	s_andn2_b64 vcc, exec, s[2:3]
	v_readfirstlane_b32 s0, v0
	s_waitcnt lgkmcnt(0)
	s_barrier
	s_cbranch_vccnz .LBB0_1425
	v_lshlrev_b32_e32 v1, 4, v0
	v_and_b32_e32 v2, 32, v0
	v_bitop3_b32 v1, v1, v2, 48 bitop3:0x6c
	v_lshrrev_b32_e32 v2, 1, v0
	v_lshrrev_b32_e32 v3, 5, v0
	v_and_b32_e32 v2, 24, v2
	v_and_b32_e32 v3, 4, v3
	v_bfe_u32 v4, v0, 2, 2
	s_lshl_b32 s3, s84, 3
	v_or3_b32 v2, v3, v4, v2
	v_lshrrev_b32_e32 v3, 3, v0
	s_lshr_b32 s1, s0, 6
	s_bfe_u32 s2, s84, 0x30003
	s_and_b32 s3, s3, 8
	v_and_or_b32 v1, v0, 64, v1
	v_and_or_b32 v4, v3, 32, v2
	s_lshr_b32 s6, s0, 8
	s_lshl_b32 s21, s1, 10
	s_or_b32 s40, s3, s2
	v_lshl_or_b32 v162, v4, 11, v1
	v_bfe_u32 v4, v0, 3, 25
	s_add_u32 s2, s82, 0x41400000
	v_or_b32_e32 v4, 64, v4
	s_movk_i32 s4, 0x60
	s_addc_u32 s3, s83, 0
	v_and_or_b32 v2, v4, s4, v2
	s_add_u32 s41, s82, 0x77400000
	v_lshl_or_b32 v164, v2, 11, v1
	v_bfe_u32 v2, v0, 2, 4
	s_movk_i32 s4, 0x70
	s_addc_u32 s42, s83, 0
	v_and_or_b32 v179, v3, 48, v2
	v_and_or_b32 v188, v4, s4, v2
	s_and_b32 s7, s84, 15
	s_add_i32 s4, 0, 0x20c00
	v_lshl_add_u32 v2, v179, 1, s4
	v_lshl_add_u32 v3, v188, 1, s4
	s_and_b64 s[4:5], s[16:17], exec
	s_cselect_b32 s4, s40, s7
	s_lshl_b32 s5, s39, 2
	s_add_i32 s5, s5, 0
	s_add_i32 s5, s5, 0x20580
	v_mov_b32_e32 v4, s5
	ds_read_b32 v4, v4
	s_waitcnt vmcnt(0)
	ds_read_u16 v5, v2
	ds_read_u16 v2, v2 offset:256
	ds_read_u16 v6, v3
	ds_read_u16 v3, v3 offset:256
	s_waitcnt lgkmcnt(4)
	v_readfirstlane_b32 s5, v4
	s_lshl_b32 s5, s5, 4
	s_or_b32 s28, s5, s4
	v_bfe_u32 v249, v0, 4, 2
	v_readlane_b32 s100, v250, 5
	v_readlane_b32 s101, v250, 6
	s_bfe_u32 s98, s28, 0x50004
	s_lshl_b32 s98, s98, 14
	s_add_u32 s100, s100, s98
	s_addc_u32 s101, s101, 0
	s_lshl_b32 s98, s28, 7
	s_and_b32 s98, s98, 0x780
	s_lshl_b32 s99, s1, 5
	s_and_b32 s99, s99, 0x60
	s_or_b32 s98, s98, s99
	v_lshl_add_u32 v248, v249, 3, s98
	v_lshlrev_b32_e32 v248, 2, v248
	v_add_u32_e32 v249, 0x2000, v248
	global_load_dwordx4 v[232:235], v248, s[100:101] offset:16
	global_load_dwordx4 v[236:239], v248, s[100:101]
	global_load_dwordx4 v[240:243], v249, s[100:101]
	global_load_dwordx4 v[244:247], v249, s[100:101] offset:16
	s_ashr_i32 s29, s28, 31
	s_lshl_b64 s[4:5], s[28:29], 19
	s_add_u32 s30, s41, s4
	s_addc_u32 s31, s42, s5
	s_add_i32 s29, s21, 0
	s_add_i32 m0, s29, 0x10000
	s_waitcnt lgkmcnt(3)
	v_lshl_or_b32 v166, v5, 11, v1
	global_load_lds_dwordx4 v162, s[30:31]
	s_add_i32 m0, s29, 0x12000
	s_add_u32 s4, s30, 0x40000
	global_load_lds_dwordx4 v164, s[30:31]
	s_addc_u32 s5, s31, 0
	s_add_i32 m0, s29, 0x14000
	s_add_i32 s43, s29, 0x2000
	global_load_lds_dwordx4 v162, s[4:5]
	s_add_i32 m0, s29, 0x16000
	s_waitcnt lgkmcnt(0)
	v_lshl_or_b32 v172, v6, 11, v1
	global_load_lds_dwordx4 v164, s[4:5]
	s_mov_b32 m0, s29
	s_add_i32 s44, s29, 0x4000
	global_load_lds_dwordx4 v166, s[2:3]
	s_mov_b32 m0, s43
	v_lshl_or_b32 v168, v2, 11, v1
	global_load_lds_dwordx4 v172, s[2:3]
	s_mov_b32 m0, s44
	s_add_i32 s45, s29, 0x6000
	v_lshl_or_b32 v170, v3, 11, v1
	global_load_lds_dwordx4 v168, s[2:3]
	s_mov_b32 m0, s45
	v_mov_b32_e32 v167, 0
	global_load_lds_dwordx4 v170, s[2:3]
	v_mov_b32_e32 v163, v167
	v_mov_b32_e32 v165, v167
	s_cmp_eq_u32 s6, 1
	s_mov_b32 s46, 0
	s_mov_b32 s47, 0x10000
	v_lshl_add_u64 v[4:5], s[30:31], 0, v[162:163]
	v_lshl_add_u64 v[2:3], s[30:31], 0, v[164:165]
	v_mov_b32_e32 v173, v167
	s_cselect_b64 s[4:5], -1, 0
	s_cmp_lg_u32 s6, 1
	s_movk_i32 s48, 0x2000
	s_cbranch_scc1 .LBB0_1406
	s_barrier

; __device__ __forceinline__ unsigned pk4_fp8_nc(float a, float b, float c, float d) { int w = 0; w = __builtin_amdgcn_cvt_pk_fp8_f32(a, b, w, false); w = __builtin_amdgcn_cvt_pk_fp8_f32(c, d, w, true); return (unsigned)w; }
; __device__ __forceinline__ float sigmoid1702(float x) { return __builtin_amdgcn_rcpf(1.0f + __builtin_amdgcn_exp2f(x * (-1.702f * 1.4426950408889634f))); }
;     __device__ __forceinline__ void operator()(const f32x4 (&acc)[2][2][4][2], const Unit& u, int wr, int wc, int fr, int fq) const {
;         const int e = u.pn >> 4, ct = u.pn & 15, row0 = u.pm * 256 + wr * 64 + fr, col = ct * 128 + wc * 32 + 8 * fq;
;         const float* bg = bgu + (size_t)e * 4096 + col; const f32x4 g0 = *(const f32x4*)bg, g1 = *(const f32x4*)(bg + 4);
;         const f32x4 u0 = (*(const f32x4*)(bg + 2048) + 1.0f) * F8_ASCALE, u1 = (*(const f32x4*)(bg + 2052) + 1.0f) * F8_ASCALE;
;         constexpr float D4 = F8_DESCALE * F8_ASCALE;
; #pragma unroll
;         for (int ai = 0; ai < 2; ++ai)
; #pragma unroll
;             for (int m = 0; m < 4; ++m) { f32x4 ga = acc[ai][0][m][0] * F8_DESCALE + g0, gb = acc[ai][0][m][1] * F8_DESCALE + g1, ua = acc[ai][1][m][0] * D4 + u0, ub = acc[ai][1][m][1] * D4 + u1;
; #pragma unroll
;                 for (int q = 0; q < 4; ++q) { float gg = fminf(ga[q], 7.0f), uu = __builtin_amdgcn_fmed3f(ua[q], -6.0f * F8_ASCALE, 8.0f * F8_ASCALE); ga[q] = uu * (gg * sigmoid1702(gg));
;                     gg = fminf(gb[q], 7.0f); uu = __builtin_amdgcn_fmed3f(ub[q], -6.0f * F8_ASCALE, 8.0f * F8_ASCALE); gb[q] = uu * (gg * sigmoid1702(gg)); }
;                 v2u w; w.x = pk4_fp8_nc(ga[0], ga[1], ga[2], ga[3]); w.y = pk4_fp8_nc(gb[0], gb[1], gb[2], gb[3]);
;                 *(v2u*)(ACT + (size_t)(row0 + ai * 128 + m * 16) * 2048 + col) = w; }
.LBB0_1419:
	s_ashr_i32 s30, s28, 4
	s_lshl_b32 s28, s28, 7
	v_readlane_b32 s64, v250, 3
	s_lshl_b32 s25, s39, 8
	s_and_b32 s28, s28, 0x780
	s_ashr_i32 s31, s30, 31
	v_readlane_b32 s66, v250, 5
	v_readlane_b32 s67, v250, 6
	v_mov_b32_e32 v15, v173
	v_mov_b32_e32 v2, v189
	s_add_i32 s25, s25, s49
	s_or_b32 s28, s28, s50
	s_lshl_b64 s[30:31], s[30:31], 14
	s_mov_b64 s[62:63], s[66:67]
	s_nop 15
	s_nop 15
	s_add_u32 s30, s62, s30
	v_lshl_add_u32 v28, v2, 3, s28
	s_addc_u32 s31, s63, s31
	v_ashrrev_i32_e32 v29, 31, v28
	v_lshl_add_u64 v[10:11], v[28:29], 2, s[30:31]
	v_add_co_u32_e32 v12, vcc, s48, v10
	v_mov_b32_e32 v2, v232
	v_mov_b32_e32 v3, v233
	v_mov_b32_e32 v4, v234
	v_mov_b32_e32 v5, v235
	v_mov_b32_e32 v6, v236
	v_mov_b32_e32 v7, v237
	v_mov_b32_e32 v8, v238
	v_mov_b32_e32 v9, v239
	v_addc_co_u32_e32 v13, vcc, 0, v11, vcc
	v_lshl_add_u64 v[10:11], v[10:11], 0, s[18:19]
	v_mov_b32_e32 v18, v240
	v_mov_b32_e32 v19, v241
	v_mov_b32_e32 v20, v242
	v_mov_b32_e32 v21, v243
	v_mov_b32_e32 v24, v244
	v_mov_b32_e32 v25, v245
	v_mov_b32_e32 v26, v246
	v_mov_b32_e32 v27, v247
	v_readlane_b32 s100, v250, 5
	v_readlane_b32 s101, v250, 6
	s_bfe_u32 s98, s24, 0x50004
	s_lshl_b32 s98, s98, 14
	s_add_u32 s100, s100, s98
	s_addc_u32 s101, s101, 0
	s_lshl_b32 s98, s24, 7
	s_and_b32 s98, s98, 0x780
	s_or_b32 s98, s98, s50
	v_lshl_add_u32 v248, v189, 3, s98
	v_lshlrev_b32_e32 v248, 2, v248
	v_add_u32_e32 v249, 0x2000, v248
	global_load_dwordx4 v[232:235], v248, s[100:101] offset:16
	global_load_dwordx4 v[236:239], v248, s[100:101]
	global_load_dwordx4 v[240:243], v249, s[100:101]
	global_load_dwordx4 v[244:247], v249, s[100:101] offset:16
	v_mov_b32_e32 v10, v150
	v_mov_b32_e32 v12, v146
	v_mov_b32_e32 v14, v151
	v_mov_b32_e32 v22, v147
	v_mov_b32_e32 v32, v148
	v_add_u32_e32 v146, s25, v15
	v_mov_b32_e32 v30, v152
	v_readlane_b32 s65, v250, 4
	v_readlane_b32 s68, v250, 7
	v_readlane_b32 s69, v250, 8
	v_readlane_b32 s70, v250, 9
	v_readlane_b32 s71, v250, 10
	s_waitcnt vmcnt(4)
	v_pk_fma_f32 v[154:155], v[154:155], s[20:21], v[2:3] op_sel_hi:[1,0,1]
	v_pk_fma_f32 v[150:151], v[160:161], s[20:21], v[8:9] op_sel_hi:[1,0,1]
	v_pk_fma_f32 v[16:17], v[158:159], s[20:21], v[6:7] op_sel_hi:[1,0,1]
	v_min_f32_e32 v148, 0x40e00000, v154
	v_min_f32_e32 v154, 0x40e00000, v155
	v_add_f32_e32 v15, 1.0, v19
	v_add_f32_e32 v23, 1.0, v25
	v_min_f32_e32 v147, 0x40e00000, v16
	v_min_f32_e32 v152, 0x40e00000, v17
	v_min_f32_e32 v150, 0x40e00000, v150
	v_pk_mul_f32 v[16:17], v[14:15], s[22:23]
	v_pk_mul_f32 v[14:15], v[22:23], s[22:23]
	v_mul_f32_e32 v22, 0xc01d265f, v154
	v_mul_f32_e32 v23, 0xc01d265f, v150
	v_exp_f32_e32 v22, v22
	v_exp_f32_e32 v23, v23
	v_add_f32_e32 v13, 1.0, v24
	v_add_f32_e32 v31, 1.0, v20
	v_add_f32_e32 v22, 1.0, v22
	v_add_f32_e32 v23, 1.0, v23
	v_rcp_f32_e32 v22, v22
	v_rcp_f32_e32 v23, v23
	v_add_f32_e32 v11, 1.0, v18
	v_pk_mul_f32 v[18:19], v[12:13], s[22:23]
	v_pk_mul_f32 v[12:13], v[30:31], s[22:23]
	v_add_f32_e32 v14, v14, v15
	v_add_f32_e32 v33, 1.0, v26
	v_mul_f32_e32 v26, 0xc01d265f, v147
	v_add_f32_e32 v12, v12, v13
	v_med3_f32 v14, v14, s57, v194
	v_mul_f32_e32 v22, v154, v22
	v_exp_f32_e32 v26, v26
	v_med3_f32 v12, v12, s57, v194
	v_mul_f32_e32 v23, v150, v23
	v_mul_f32_e32 v14, v14, v22
	v_min_f32_e32 v22, 0x40e00000, v151
	v_pk_fma_f32 v[156:157], v[156:157], s[20:21], v[4:5] op_sel_hi:[1,0,1]
	v_mul_f32_e32 v12, v12, v23
	v_mul_f32_e32 v23, 0xc01d265f, v22
	v_min_f32_e32 v20, 0x40e00000, v156
	v_exp_f32_e32 v23, v23
	v_mul_f32_e32 v30, 0xc01d265f, v20
	v_exp_f32_e32 v30, v30
	v_add_f32_e32 v26, 1.0, v26
	v_rcp_f32_e32 v26, v26
	v_add_f32_e32 v23, 1.0, v23
	v_pk_mul_f32 v[24:25], v[10:11], s[22:23]
	v_mul_f32_e32 v155, 0xc01d265f, v148
	v_mul_f32_e32 v156, 0xc01d265f, v152
	v_rcp_f32_e32 v23, v23
	v_pk_mul_f32 v[10:11], v[32:33], s[22:23]
	v_add_f32_e32 v24, v24, v25
	v_exp_f32_e32 v31, v155
	v_exp_f32_e32 v32, v156
	v_add_f32_e32 v30, 1.0, v30
	v_med3_f32 v24, v24, s57, v194
	v_rcp_f32_e32 v30, v30
	v_mul_f32_e32 v26, v147, v26
	v_mul_f32_e32 v24, v24, v26
	v_min_f32_e32 v26, 0x40e00000, v157
	v_mul_f32_e32 v22, v22, v23
	v_add_f32_e32 v23, 1.0, v27
	v_mul_f32_e32 v27, 0xc01d265f, v26
	v_add_f32_e32 v10, v10, v11
	v_add_f32_e32 v31, 1.0, v31
	v_add_f32_e32 v32, 1.0, v32
	v_exp_f32_e32 v27, v27
	v_rcp_f32_e32 v31, v31
	v_rcp_f32_e32 v32, v32
	v_med3_f32 v10, v10, s57, v194
	v_mul_f32_e32 v20, v20, v30
	v_mul_f32_e32 v10, v10, v20
	v_add_f32_e32 v21, 1.0, v21
	v_mov_b32_e32 v20, v153
	v_pk_mul_f32 v[20:21], v[20:21], s[22:23]
	v_add_f32_e32 v18, v18, v19
	v_add_f32_e32 v16, v16, v17
	v_add_f32_e32 v20, v20, v21
	v_add_f32_e32 v27, 1.0, v27
	v_med3_f32 v18, v18, s57, v194
	v_med3_f32 v16, v16, s57, v194
	v_mul_f32_e32 v31, v148, v31
	v_mul_f32_e32 v32, v152, v32
	v_med3_f32 v20, v20, s57, v194
	v_rcp_f32_e32 v27, v27
	v_mul_f32_e32 v18, v18, v31
	v_mul_f32_e32 v16, v16, v32
	v_mul_f32_e32 v20, v20, v22
	v_mov_b32_e32 v22, v149
	v_mov_b32_e32 v30, v167
	v_mov_b32_e32 v31, v167
	v_pk_mul_f32 v[22:23], v[22:23], s[22:23]
	v_cvt_pk_fp8_f32 v30, v24, v16
	v_cvt_pk_fp8_f32 v31, v18, v14
	v_add_f32_e32 v22, v22, v23
	v_med3_f32 v22, v22, s57, v194
	v_mul_f32_e32 v14, v26, v27
	v_mul_f32_e32 v14, v22, v14
	v_cvt_pk_fp8_f32 v30, v12, v20 op_sel:[0,0,1]
	v_cvt_pk_fp8_f32 v31, v10, v14 op_sel:[0,0,1]
	v_ashrrev_i32_e32 v147, 31, v146
	v_lshlrev_b64 v[26:27], 11, v[146:147]
	v_lshl_add_u64 v[26:27], s[6:7], 0, v[26:27]
	v_lshl_add_u64 v[26:27], v[26:27], 0, v[28:29]
	global_store_dwordx2 v[26:27], v[30:31], off
	v_pk_fma_f32 v[30:31], v[142:143], s[20:21], v[6:7] op_sel_hi:[1,0,1]
	v_pk_fma_f32 v[138:139], v[138:139], s[20:21], v[2:3] op_sel_hi:[1,0,1]
; __device__ __forceinline__ unsigned pk4_fp8_nc(float a, float b, float c, float d) { int w = 0; w = __builtin_amdgcn_cvt_pk_fp8_f32(a, b, w, false); w = __builtin_amdgcn_cvt_pk_fp8_f32(c, d, w, true); return (unsigned)w; }
; __device__ __forceinline__ float sigmoid1702(float x) { return __builtin_amdgcn_rcpf(1.0f + __builtin_amdgcn_exp2f(x * (-1.702f * 1.4426950408889634f))); }
;     __device__ __forceinline__ void operator()(const f32x4 (&acc)[2][2][4][2], const Unit& u, int wr, int wc, int fr, int fq) const {
;     ...
;         for (int ai = 0; ai < 2; ++ai)
; #pragma unroll
;             for (int m = 0; m < 4; ++m) { f32x4 ga = acc[ai][0][m][0] * F8_DESCALE + g0, gb = acc[ai][0][m][1] * F8_DESCALE + g1, ua = acc[ai][1][m][0] * D4 + u0, ub = acc[ai][1][m][1] * D4 + u1;
; #pragma unroll
;                 for (int q = 0; q < 4; ++q) { float gg = fminf(ga[q], 7.0f), uu = __builtin_amdgcn_fmed3f(ua[q], -6.0f * F8_ASCALE, 8.0f * F8_ASCALE); ga[q] = uu * (gg * sigmoid1702(gg));
;                     gg = fminf(gb[q], 7.0f); uu = __builtin_amdgcn_fmed3f(ub[q], -6.0f * F8_ASCALE, 8.0f * F8_ASCALE); gb[q] = uu * (gg * sigmoid1702(gg)); }
;                 v2u w; w.x = pk4_fp8_nc(ga[0], ga[1], ga[2], ga[3]); w.y = pk4_fp8_nc(gb[0], gb[1], gb[2], gb[3]);
;                 *(v2u*)(ACT + (size_t)(row0 + ai * 128 + m * 16) * 2048 + col) = w; }
	v_min_f32_e32 v10, 0x40e00000, v30
	v_mul_f32_e32 v12, 0xc01d265f, v10
	v_exp_f32_e32 v12, v12
	v_min_f32_e32 v16, 0x40e00000, v138
	v_mul_f32_e32 v18, 0xc01d265f, v16
	v_exp_f32_e32 v18, v18
	v_add_f32_e32 v12, 1.0, v12
	v_rcp_f32_e32 v12, v12
	v_fmamk_f32 v14, v134, 0x3b800000, v25
	v_med3_f32 v14, v14, s57, v194
	v_fmamk_f32 v20, v126, 0x3b800000, v19
	v_mul_f32_e32 v10, v10, v12
	v_mul_f32_e32 v10, v14, v10
	v_min_f32_e32 v14, 0x40e00000, v31
	v_add_f32_e32 v12, 1.0, v18
	v_mul_f32_e32 v18, 0xc01d265f, v14
	v_rcp_f32_e32 v12, v12
	v_exp_f32_e32 v18, v18
	v_med3_f32 v20, v20, s57, v194
	v_pk_fma_f32 v[28:29], v[144:145], s[20:21], v[8:9] op_sel_hi:[1,0,1]
	v_mul_f32_e32 v12, v16, v12
	v_add_f32_e32 v16, 1.0, v18
	v_rcp_f32_e32 v16, v16
	v_mul_f32_e32 v12, v20, v12
	v_min_f32_e32 v22, 0x40e00000, v28
	v_mul_f32_e32 v24, 0xc01d265f, v22
	v_mul_f32_e32 v14, v14, v16
	v_min_f32_e32 v16, 0x40e00000, v139
	v_mul_f32_e32 v20, 0xc01d265f, v16
	v_exp_f32_e32 v20, v20
	v_exp_f32_e32 v24, v24
	v_pk_fma_f32 v[32:33], v[140:141], s[20:21], v[4:5] op_sel_hi:[1,0,1]
	v_fmamk_f32 v18, v135, 0x3b800000, v17
	v_add_f32_e32 v20, 1.0, v20
	v_rcp_f32_e32 v20, v20
	v_med3_f32 v18, v18, s57, v194
	v_mul_f32_e32 v14, v18, v14
	v_fmamk_f32 v18, v127, 0x3b800000, v15
	v_mul_f32_e32 v16, v16, v20
	v_add_f32_e32 v20, 1.0, v24
	v_min_f32_e32 v24, 0x40e00000, v32
	v_rcp_f32_e32 v20, v20
	v_mul_f32_e32 v28, 0xc01d265f, v24
	v_exp_f32_e32 v28, v28
	v_med3_f32 v18, v18, s57, v194
	v_mul_f32_e32 v16, v18, v16
	v_fmamk_f32 v18, v136, 0x3b800000, v13
	v_med3_f32 v18, v18, s57, v194
	v_mul_f32_e32 v20, v22, v20
	v_min_f32_e32 v22, 0x40e00000, v29
	v_mul_f32_e32 v18, v18, v20
	v_add_f32_e32 v20, 1.0, v28
	v_mul_f32_e32 v28, 0xc01d265f, v22
	v_rcp_f32_e32 v20, v20
	v_exp_f32_e32 v28, v28
	v_fmamk_f32 v29, v128, 0x3b800000, v11
	v_med3_f32 v29, v29, s57, v194
	v_mul_f32_e32 v20, v24, v20
	v_add_f32_e32 v24, 1.0, v28
	v_rcp_f32_e32 v24, v24
	v_mul_f32_e32 v20, v29, v20
	v_fmamk_f32 v28, v137, 0x3b800000, v21
	v_med3_f32 v28, v28, s57, v194
	v_mul_f32_e32 v22, v22, v24
	v_min_f32_e32 v24, 0x40e00000, v33
	v_mul_f32_e32 v29, 0xc01d265f, v24
	v_exp_f32_e32 v29, v29
	v_mul_f32_e32 v22, v28, v22
	v_fmamk_f32 v28, v129, 0x3b800000, v23
	v_med3_f32 v30, v28, s57, v194
	v_add_f32_e32 v28, 1.0, v29
	v_rcp_f32_e32 v31, v28
	v_mov_b32_e32 v28, v167
	v_mov_b32_e32 v29, v167
	v_cvt_pk_fp8_f32 v28, v10, v14
	v_cvt_pk_fp8_f32 v29, v12, v16
	v_mul_f32_e32 v10, v24, v31
	v_mul_f32_e32 v10, v30, v10
	v_cvt_pk_fp8_f32 v28, v18, v22 op_sel:[0,0,1]
	v_cvt_pk_fp8_f32 v29, v20, v10 op_sel:[0,0,1]
	v_add_co_u32_e32 v30, vcc, s54, v26
	v_pk_fma_f32 v[122:123], v[122:123], s[20:21], v[2:3] op_sel_hi:[1,0,1]
	s_nop 0
	v_addc_co_u32_e32 v31, vcc, 0, v27, vcc
	global_store_dwordx2 v[30:31], v[28:29], off
	v_pk_fma_f32 v[30:31], v[130:131], s[20:21], v[6:7] op_sel_hi:[1,0,1]
	v_min_f32_e32 v16, 0x40e00000, v122
	v_min_f32_e32 v10, 0x40e00000, v30
	v_mul_f32_e32 v12, 0xc01d265f, v10
	v_exp_f32_e32 v12, v12
	v_mul_f32_e32 v18, 0xc01d265f, v16
	v_exp_f32_e32 v18, v18
	v_fmamk_f32 v14, v118, 0x3b800000, v25
	v_add_f32_e32 v12, 1.0, v12
	v_rcp_f32_e32 v12, v12
	v_med3_f32 v14, v14, s57, v194
	v_fmamk_f32 v20, v110, 0x3b800000, v19
	v_med3_f32 v20, v20, s57, v194
	v_mul_f32_e32 v10, v10, v12
	v_mul_f32_e32 v10, v14, v10
	v_min_f32_e32 v14, 0x40e00000, v31
	v_add_f32_e32 v12, 1.0, v18
	v_mul_f32_e32 v18, 0xc01d265f, v14
	v_rcp_f32_e32 v12, v12
	v_exp_f32_e32 v18, v18
	v_pk_fma_f32 v[28:29], v[132:133], s[20:21], v[8:9] op_sel_hi:[1,0,1]
	v_pk_fma_f32 v[32:33], v[124:125], s[20:21], v[4:5] op_sel_hi:[1,0,1]
	v_mul_f32_e32 v12, v16, v12
	v_add_f32_e32 v16, 1.0, v18
	v_rcp_f32_e32 v16, v16
	v_mul_f32_e32 v12, v20, v12
	v_min_f32_e32 v22, 0x40e00000, v28
	v_mul_f32_e32 v24, 0xc01d265f, v22
	v_mul_f32_e32 v14, v14, v16
	v_min_f32_e32 v16, 0x40e00000, v123
	v_mul_f32_e32 v20, 0xc01d265f, v16
	v_exp_f32_e32 v20, v20
	v_exp_f32_e32 v24, v24
	v_fmamk_f32 v18, v119, 0x3b800000, v17
	v_med3_f32 v18, v18, s57, v194
	v_add_f32_e32 v20, 1.0, v20
	v_rcp_f32_e32 v20, v20
	v_mul_f32_e32 v14, v18, v14
	v_fmamk_f32 v18, v111, 0x3b800000, v15
	v_med3_f32 v18, v18, s57, v194
	v_mul_f32_e32 v16, v16, v20
	v_add_f32_e32 v20, 1.0, v24
	v_min_f32_e32 v24, 0x40e00000, v32
	v_rcp_f32_e32 v20, v20
	v_mul_f32_e32 v28, 0xc01d265f, v24
	v_exp_f32_e32 v28, v28
	v_mul_f32_e32 v16, v18, v16
	v_fmamk_f32 v18, v120, 0x3b800000, v13
	v_med3_f32 v18, v18, s57, v194
	v_mul_f32_e32 v20, v22, v20
	v_min_f32_e32 v22, 0x40e00000, v29
	v_mul_f32_e32 v18, v18, v20
	v_add_f32_e32 v20, 1.0, v28
	v_mul_f32_e32 v28, 0xc01d265f, v22
	v_rcp_f32_e32 v20, v20
	v_exp_f32_e32 v28, v28
	v_fmamk_f32 v29, v112, 0x3b800000, v11
	v_med3_f32 v29, v29, s57, v194
	v_mul_f32_e32 v20, v24, v20
	v_add_f32_e32 v24, 1.0, v28
	v_rcp_f32_e32 v24, v24
	v_mul_f32_e32 v20, v29, v20
	v_fmamk_f32 v28, v121, 0x3b800000, v21
	v_med3_f32 v28, v28, s57, v194
	v_mul_f32_e32 v22, v22, v24
	v_min_f32_e32 v24, 0x40e00000, v33
	v_mul_f32_e32 v29, 0xc01d265f, v24
	v_exp_f32_e32 v29, v29
	v_mul_f32_e32 v22, v28, v22
	v_fmamk_f32 v28, v113, 0x3b800000, v23
	v_med3_f32 v30, v28, s57, v194
	v_add_f32_e32 v28, 1.0, v29
	v_rcp_f32_e32 v31, v28
	v_mov_b32_e32 v28, v167
	v_mov_b32_e32 v29, v167
	v_cvt_pk_fp8_f32 v28, v10, v14
	v_cvt_pk_fp8_f32 v29, v12, v16
	v_mul_f32_e32 v10, v24, v31
	v_mul_f32_e32 v10, v30, v10
	v_cvt_pk_fp8_f32 v28, v18, v22 op_sel:[0,0,1]
	v_cvt_pk_fp8_f32 v29, v20, v10 op_sel:[0,0,1]
	v_add_co_u32_e32 v30, vcc, s47, v26
	v_pk_fma_f32 v[106:107], v[106:107], s[20:21], v[2:3] op_sel_hi:[1,0,1]
	s_nop 0
	v_addc_co_u32_e32 v31, vcc, 0, v27, vcc
	global_store_dwordx2 v[30:31], v[28:29], off
; __device__ __forceinline__ unsigned pk4_fp8_nc(float a, float b, float c, float d) { int w = 0; w = __builtin_amdgcn_cvt_pk_fp8_f32(a, b, w, false); w = __builtin_amdgcn_cvt_pk_fp8_f32(c, d, w, true); return (unsigned)w; }
; __device__ __forceinline__ float sigmoid1702(float x) { return __builtin_amdgcn_rcpf(1.0f + __builtin_amdgcn_exp2f(x * (-1.702f * 1.4426950408889634f))); }
;     __device__ __forceinline__ void operator()(const f32x4 (&acc)[2][2][4][2], const Unit& u, int wr, int wc, int fr, int fq) const {
;     ...
;         for (int ai = 0; ai < 2; ++ai)
; #pragma unroll
;             for (int m = 0; m < 4; ++m) { f32x4 ga = acc[ai][0][m][0] * F8_DESCALE + g0, gb = acc[ai][0][m][1] * F8_DESCALE + g1, ua = acc[ai][1][m][0] * D4 + u0, ub = acc[ai][1][m][1] * D4 + u1;
; #pragma unroll
;                 for (int q = 0; q < 4; ++q) { float gg = fminf(ga[q], 7.0f), uu = __builtin_amdgcn_fmed3f(ua[q], -6.0f * F8_ASCALE, 8.0f * F8_ASCALE); ga[q] = uu * (gg * sigmoid1702(gg));
;                     gg = fminf(gb[q], 7.0f); uu = __builtin_amdgcn_fmed3f(ub[q], -6.0f * F8_ASCALE, 8.0f * F8_ASCALE); gb[q] = uu * (gg * sigmoid1702(gg)); }
;                 v2u w; w.x = pk4_fp8_nc(ga[0], ga[1], ga[2], ga[3]); w.y = pk4_fp8_nc(gb[0], gb[1], gb[2], gb[3]);
;                 *(v2u*)(ACT + (size_t)(row0 + ai * 128 + m * 16) * 2048 + col) = w; }
	v_pk_fma_f32 v[30:31], v[114:115], s[20:21], v[6:7] op_sel_hi:[1,0,1]
	v_min_f32_e32 v16, 0x40e00000, v106
	v_min_f32_e32 v10, 0x40e00000, v30
	v_mul_f32_e32 v12, 0xc01d265f, v10
	v_exp_f32_e32 v12, v12
	v_mul_f32_e32 v18, 0xc01d265f, v16
	v_exp_f32_e32 v18, v18
	v_fmamk_f32 v14, v102, 0x3b800000, v25
	v_add_f32_e32 v12, 1.0, v12
	v_rcp_f32_e32 v12, v12
	v_med3_f32 v14, v14, s57, v194
	v_fmamk_f32 v20, v98, 0x3b800000, v19
	v_med3_f32 v20, v20, s57, v194
	v_mul_f32_e32 v10, v10, v12
	v_mul_f32_e32 v10, v14, v10
	v_min_f32_e32 v14, 0x40e00000, v31
	v_add_f32_e32 v12, 1.0, v18
	v_mul_f32_e32 v18, 0xc01d265f, v14
	v_rcp_f32_e32 v12, v12
	v_exp_f32_e32 v18, v18
	v_pk_fma_f32 v[28:29], v[116:117], s[20:21], v[8:9] op_sel_hi:[1,0,1]
	v_pk_fma_f32 v[32:33], v[108:109], s[20:21], v[4:5] op_sel_hi:[1,0,1]
	v_mul_f32_e32 v12, v16, v12
	v_add_f32_e32 v16, 1.0, v18
	v_rcp_f32_e32 v16, v16
	v_mul_f32_e32 v12, v20, v12
	v_min_f32_e32 v22, 0x40e00000, v28
	v_mul_f32_e32 v24, 0xc01d265f, v22
	v_mul_f32_e32 v14, v14, v16
	v_min_f32_e32 v16, 0x40e00000, v107
	v_mul_f32_e32 v20, 0xc01d265f, v16
	v_exp_f32_e32 v20, v20
	v_exp_f32_e32 v24, v24
	v_fmamk_f32 v18, v103, 0x3b800000, v17
	v_med3_f32 v18, v18, s57, v194
	v_add_f32_e32 v20, 1.0, v20
	v_rcp_f32_e32 v20, v20
	v_mul_f32_e32 v14, v18, v14
	v_fmamk_f32 v18, v99, 0x3b800000, v15
	v_med3_f32 v18, v18, s57, v194
	v_mul_f32_e32 v16, v16, v20
	v_add_f32_e32 v20, 1.0, v24
	v_min_f32_e32 v24, 0x40e00000, v32
	v_rcp_f32_e32 v20, v20
	v_mul_f32_e32 v28, 0xc01d265f, v24
	v_exp_f32_e32 v28, v28
	v_mul_f32_e32 v16, v18, v16
	v_fmamk_f32 v18, v104, 0x3b800000, v13
	v_med3_f32 v18, v18, s57, v194
	v_mul_f32_e32 v20, v22, v20
	v_min_f32_e32 v22, 0x40e00000, v29
	v_mul_f32_e32 v18, v18, v20
	v_add_f32_e32 v20, 1.0, v28
	v_mul_f32_e32 v28, 0xc01d265f, v22
	v_rcp_f32_e32 v20, v20
	v_exp_f32_e32 v28, v28
	v_fmamk_f32 v29, v100, 0x3b800000, v11
	v_med3_f32 v29, v29, s57, v194
	v_mul_f32_e32 v20, v24, v20
	v_add_f32_e32 v24, 1.0, v28
	v_rcp_f32_e32 v24, v24
	v_mul_f32_e32 v20, v29, v20
	v_fmamk_f32 v28, v105, 0x3b800000, v21
	v_med3_f32 v28, v28, s57, v194
	v_mul_f32_e32 v22, v22, v24
	v_min_f32_e32 v24, 0x40e00000, v33
	v_mul_f32_e32 v29, 0xc01d265f, v24
	v_exp_f32_e32 v29, v29
	v_mul_f32_e32 v22, v28, v22
	v_fmamk_f32 v28, v101, 0x3b800000, v23
	v_med3_f32 v30, v28, s57, v194
	v_add_f32_e32 v28, 1.0, v29
	v_rcp_f32_e32 v31, v28
	v_mov_b32_e32 v28, v167
	v_mov_b32_e32 v29, v167
	v_cvt_pk_fp8_f32 v28, v10, v14
	v_cvt_pk_fp8_f32 v29, v12, v16
	v_mul_f32_e32 v10, v24, v31
	v_mul_f32_e32 v10, v30, v10
	v_cvt_pk_fp8_f32 v28, v18, v22 op_sel:[0,0,1]
	v_cvt_pk_fp8_f32 v29, v20, v10 op_sel:[0,0,1]
	v_add_co_u32_e32 v30, vcc, s53, v26
	v_pk_fma_f32 v[90:91], v[90:91], s[20:21], v[2:3] op_sel_hi:[1,0,1]
	s_nop 0
	v_addc_co_u32_e32 v31, vcc, 0, v27, vcc
	global_store_dwordx2 v[30:31], v[28:29], off
	v_pk_fma_f32 v[30:31], v[94:95], s[20:21], v[6:7] op_sel_hi:[1,0,1]
	v_min_f32_e32 v16, 0x40e00000, v90
	v_min_f32_e32 v10, 0x40e00000, v30
	v_mul_f32_e32 v12, 0xc01d265f, v10
	v_exp_f32_e32 v12, v12
	v_mul_f32_e32 v18, 0xc01d265f, v16
	v_exp_f32_e32 v18, v18
	v_fmamk_f32 v14, v86, 0x3b800000, v25
	v_add_f32_e32 v12, 1.0, v12
	v_rcp_f32_e32 v12, v12
	v_med3_f32 v14, v14, s57, v194
	v_fmamk_f32 v20, v78, 0x3b800000, v19
	v_med3_f32 v20, v20, s57, v194
	v_mul_f32_e32 v10, v10, v12
	v_mul_f32_e32 v10, v14, v10
	v_min_f32_e32 v14, 0x40e00000, v31
	v_add_f32_e32 v12, 1.0, v18
	v_mul_f32_e32 v18, 0xc01d265f, v14
	v_rcp_f32_e32 v12, v12
	v_exp_f32_e32 v18, v18
	v_pk_fma_f32 v[28:29], v[96:97], s[20:21], v[8:9] op_sel_hi:[1,0,1]
	v_pk_fma_f32 v[32:33], v[92:93], s[20:21], v[4:5] op_sel_hi:[1,0,1]
	v_mul_f32_e32 v12, v16, v12
	v_add_f32_e32 v16, 1.0, v18
	v_rcp_f32_e32 v16, v16
	v_mul_f32_e32 v12, v20, v12
	v_min_f32_e32 v22, 0x40e00000, v28
	v_mul_f32_e32 v24, 0xc01d265f, v22
	v_mul_f32_e32 v14, v14, v16
	v_min_f32_e32 v16, 0x40e00000, v91
	v_mul_f32_e32 v20, 0xc01d265f, v16
	v_exp_f32_e32 v20, v20
	v_exp_f32_e32 v24, v24
	v_fmamk_f32 v18, v87, 0x3b800000, v17
	v_med3_f32 v18, v18, s57, v194
	v_add_f32_e32 v20, 1.0, v20
	v_rcp_f32_e32 v20, v20
	v_mul_f32_e32 v14, v18, v14
	v_fmamk_f32 v18, v79, 0x3b800000, v15
	v_med3_f32 v18, v18, s57, v194
	v_mul_f32_e32 v16, v16, v20
	v_add_f32_e32 v20, 1.0, v24
	v_min_f32_e32 v24, 0x40e00000, v32
	v_rcp_f32_e32 v20, v20
	v_mul_f32_e32 v28, 0xc01d265f, v24
	v_exp_f32_e32 v28, v28
	v_mul_f32_e32 v16, v18, v16
	v_fmamk_f32 v18, v88, 0x3b800000, v13
	v_med3_f32 v18, v18, s57, v194
	v_mul_f32_e32 v20, v22, v20
	v_min_f32_e32 v22, 0x40e00000, v29
	v_mul_f32_e32 v18, v18, v20
	v_add_f32_e32 v20, 1.0, v28
	v_mul_f32_e32 v28, 0xc01d265f, v22
	v_rcp_f32_e32 v20, v20
	v_exp_f32_e32 v28, v28
	v_fmamk_f32 v29, v80, 0x3b800000, v11
	v_med3_f32 v29, v29, s57, v194
	v_mul_f32_e32 v20, v24, v20
	v_add_f32_e32 v24, 1.0, v28
	v_rcp_f32_e32 v24, v24
	v_mul_f32_e32 v20, v29, v20
	v_fmamk_f32 v28, v89, 0x3b800000, v21
	v_med3_f32 v28, v28, s57, v194
	v_mul_f32_e32 v22, v22, v24
	v_min_f32_e32 v24, 0x40e00000, v33
	v_mul_f32_e32 v29, 0xc01d265f, v24
	v_exp_f32_e32 v29, v29
	v_mul_f32_e32 v22, v28, v22
	v_fmamk_f32 v28, v81, 0x3b800000, v23
	v_med3_f32 v30, v28, s57, v194
	v_add_f32_e32 v28, 1.0, v29
	v_rcp_f32_e32 v31, v28
	v_mov_b32_e32 v28, v167
	v_mov_b32_e32 v29, v167
	v_cvt_pk_fp8_f32 v28, v10, v14
	v_cvt_pk_fp8_f32 v29, v12, v16
	v_mul_f32_e32 v10, v24, v31
	v_mul_f32_e32 v10, v30, v10
	v_cvt_pk_fp8_f32 v28, v18, v22 op_sel:[0,0,1]
	v_cvt_pk_fp8_f32 v29, v20, v10 op_sel:[0,0,1]
	v_add_co_u32_e32 v30, vcc, s58, v26
	v_pk_fma_f32 v[74:75], v[74:75], s[20:21], v[2:3] op_sel_hi:[1,0,1]
	s_nop 0
	v_addc_co_u32_e32 v31, vcc, 0, v27, vcc
; __device__ __forceinline__ unsigned pk4_fp8_nc(float a, float b, float c, float d) { int w = 0; w = __builtin_amdgcn_cvt_pk_fp8_f32(a, b, w, false); w = __builtin_amdgcn_cvt_pk_fp8_f32(c, d, w, true); return (unsigned)w; }
; __device__ __forceinline__ float sigmoid1702(float x) { return __builtin_amdgcn_rcpf(1.0f + __builtin_amdgcn_exp2f(x * (-1.702f * 1.4426950408889634f))); }
;     __device__ __forceinline__ void operator()(const f32x4 (&acc)[2][2][4][2], const Unit& u, int wr, int wc, int fr, int fq) const {
;     ...
;         for (int ai = 0; ai < 2; ++ai)
; #pragma unroll
;             for (int m = 0; m < 4; ++m) { f32x4 ga = acc[ai][0][m][0] * F8_DESCALE + g0, gb = acc[ai][0][m][1] * F8_DESCALE + g1, ua = acc[ai][1][m][0] * D4 + u0, ub = acc[ai][1][m][1] * D4 + u1;
; #pragma unroll
;                 for (int q = 0; q < 4; ++q) { float gg = fminf(ga[q], 7.0f), uu = __builtin_amdgcn_fmed3f(ua[q], -6.0f * F8_ASCALE, 8.0f * F8_ASCALE); ga[q] = uu * (gg * sigmoid1702(gg));
;                     gg = fminf(gb[q], 7.0f); uu = __builtin_amdgcn_fmed3f(ub[q], -6.0f * F8_ASCALE, 8.0f * F8_ASCALE); gb[q] = uu * (gg * sigmoid1702(gg)); }
;                 v2u w; w.x = pk4_fp8_nc(ga[0], ga[1], ga[2], ga[3]); w.y = pk4_fp8_nc(gb[0], gb[1], gb[2], gb[3]);
;                 *(v2u*)(ACT + (size_t)(row0 + ai * 128 + m * 16) * 2048 + col) = w; }
	global_store_dwordx2 v[30:31], v[28:29], off
	v_pk_fma_f32 v[30:31], v[82:83], s[20:21], v[6:7] op_sel_hi:[1,0,1]
	v_min_f32_e32 v16, 0x40e00000, v74
	v_min_f32_e32 v10, 0x40e00000, v30
	v_mul_f32_e32 v12, 0xc01d265f, v10
	v_exp_f32_e32 v12, v12
	v_mul_f32_e32 v18, 0xc01d265f, v16
	v_exp_f32_e32 v18, v18
	v_fmamk_f32 v14, v70, 0x3b800000, v25
	v_add_f32_e32 v12, 1.0, v12
	v_rcp_f32_e32 v12, v12
	v_med3_f32 v14, v14, s57, v194
	v_fmamk_f32 v20, v62, 0x3b800000, v19
	v_med3_f32 v20, v20, s57, v194
	v_mul_f32_e32 v10, v10, v12
	v_mul_f32_e32 v10, v14, v10
	v_min_f32_e32 v14, 0x40e00000, v31
	v_add_f32_e32 v12, 1.0, v18
	v_mul_f32_e32 v18, 0xc01d265f, v14
	v_rcp_f32_e32 v12, v12
	v_exp_f32_e32 v18, v18
	v_pk_fma_f32 v[28:29], v[84:85], s[20:21], v[8:9] op_sel_hi:[1,0,1]
	v_pk_fma_f32 v[32:33], v[76:77], s[20:21], v[4:5] op_sel_hi:[1,0,1]
	v_mul_f32_e32 v12, v16, v12
	v_add_f32_e32 v16, 1.0, v18
	v_rcp_f32_e32 v16, v16
	v_mul_f32_e32 v12, v20, v12
	v_min_f32_e32 v22, 0x40e00000, v28
	v_mul_f32_e32 v24, 0xc01d265f, v22
	v_mul_f32_e32 v14, v14, v16
	v_min_f32_e32 v16, 0x40e00000, v75
	v_mul_f32_e32 v20, 0xc01d265f, v16
	v_exp_f32_e32 v20, v20
	v_exp_f32_e32 v24, v24
	v_fmamk_f32 v18, v71, 0x3b800000, v17
	v_med3_f32 v18, v18, s57, v194
	v_add_f32_e32 v20, 1.0, v20
	v_rcp_f32_e32 v20, v20
	v_mul_f32_e32 v14, v18, v14
	v_fmamk_f32 v18, v63, 0x3b800000, v15
	v_med3_f32 v18, v18, s57, v194
	v_mul_f32_e32 v16, v16, v20
	v_add_f32_e32 v20, 1.0, v24
	v_min_f32_e32 v24, 0x40e00000, v32
	v_rcp_f32_e32 v20, v20
	v_mul_f32_e32 v28, 0xc01d265f, v24
	v_exp_f32_e32 v28, v28
	v_mul_f32_e32 v16, v18, v16
	v_fmamk_f32 v18, v72, 0x3b800000, v13
	v_med3_f32 v18, v18, s57, v194
	v_mul_f32_e32 v20, v22, v20
	v_min_f32_e32 v22, 0x40e00000, v29
	v_mul_f32_e32 v18, v18, v20
	v_add_f32_e32 v20, 1.0, v28
	v_mul_f32_e32 v28, 0xc01d265f, v22
	v_rcp_f32_e32 v20, v20
	v_exp_f32_e32 v28, v28
	v_fmamk_f32 v29, v64, 0x3b800000, v11
	v_med3_f32 v29, v29, s57, v194
	v_mul_f32_e32 v20, v24, v20
	v_add_f32_e32 v24, 1.0, v28
	v_rcp_f32_e32 v24, v24
	v_mul_f32_e32 v20, v29, v20
	v_fmamk_f32 v28, v73, 0x3b800000, v21
	v_med3_f32 v28, v28, s57, v194
	v_mul_f32_e32 v22, v22, v24
	v_min_f32_e32 v24, 0x40e00000, v33
	v_mul_f32_e32 v29, 0xc01d265f, v24
	v_exp_f32_e32 v29, v29
	v_mul_f32_e32 v22, v28, v22
	v_fmamk_f32 v28, v65, 0x3b800000, v23
	v_med3_f32 v30, v28, s57, v194
	v_add_f32_e32 v28, 1.0, v29
	v_rcp_f32_e32 v31, v28
	v_mov_b32_e32 v28, v167
	v_mov_b32_e32 v29, v167
	v_cvt_pk_fp8_f32 v28, v10, v14
	v_cvt_pk_fp8_f32 v29, v12, v16
	v_mul_f32_e32 v10, v24, v31
	v_mul_f32_e32 v10, v30, v10
	v_cvt_pk_fp8_f32 v28, v18, v22 op_sel:[0,0,1]
	v_cvt_pk_fp8_f32 v29, v20, v10 op_sel:[0,0,1]
	v_add_co_u32_e32 v30, vcc, s59, v26
	v_pk_fma_f32 v[58:59], v[58:59], s[20:21], v[2:3] op_sel_hi:[1,0,1]
	s_nop 0
	v_addc_co_u32_e32 v31, vcc, 0, v27, vcc
	global_store_dwordx2 v[30:31], v[28:29], off
	v_pk_fma_f32 v[30:31], v[66:67], s[20:21], v[6:7] op_sel_hi:[1,0,1]
	v_min_f32_e32 v16, 0x40e00000, v58
	v_min_f32_e32 v10, 0x40e00000, v30
	v_mul_f32_e32 v12, 0xc01d265f, v10
	v_exp_f32_e32 v12, v12
	v_mul_f32_e32 v18, 0xc01d265f, v16
	v_exp_f32_e32 v18, v18
	v_fmamk_f32 v14, v54, 0x3b800000, v25
	v_add_f32_e32 v12, 1.0, v12
	v_rcp_f32_e32 v12, v12
	v_med3_f32 v14, v14, s57, v194
	v_fmamk_f32 v20, v46, 0x3b800000, v19
	v_med3_f32 v20, v20, s57, v194
	v_mul_f32_e32 v10, v10, v12
	v_mul_f32_e32 v10, v14, v10
	v_min_f32_e32 v14, 0x40e00000, v31
	v_add_f32_e32 v12, 1.0, v18
	v_mul_f32_e32 v18, 0xc01d265f, v14
	v_rcp_f32_e32 v12, v12
	v_exp_f32_e32 v18, v18
	v_pk_fma_f32 v[28:29], v[68:69], s[20:21], v[8:9] op_sel_hi:[1,0,1]
	v_pk_fma_f32 v[32:33], v[60:61], s[20:21], v[4:5] op_sel_hi:[1,0,1]
	v_mul_f32_e32 v12, v16, v12
	v_add_f32_e32 v16, 1.0, v18
	v_rcp_f32_e32 v16, v16
	v_mul_f32_e32 v12, v20, v12
	v_min_f32_e32 v22, 0x40e00000, v28
	v_mul_f32_e32 v24, 0xc01d265f, v22
	v_mul_f32_e32 v14, v14, v16
	v_min_f32_e32 v16, 0x40e00000, v59
	v_mul_f32_e32 v20, 0xc01d265f, v16
	v_exp_f32_e32 v20, v20
	v_exp_f32_e32 v24, v24
	v_fmamk_f32 v18, v55, 0x3b800000, v17
	v_med3_f32 v18, v18, s57, v194
	v_add_f32_e32 v20, 1.0, v20
	v_rcp_f32_e32 v20, v20
	v_mul_f32_e32 v14, v18, v14
	v_fmamk_f32 v18, v47, 0x3b800000, v15
	v_med3_f32 v18, v18, s57, v194
	v_mul_f32_e32 v16, v16, v20
; __device__ __forceinline__ unsigned pk4_fp8_nc(float a, float b, float c, float d) { int w = 0; w = __builtin_amdgcn_cvt_pk_fp8_f32(a, b, w, false); w = __builtin_amdgcn_cvt_pk_fp8_f32(c, d, w, true); return (unsigned)w; }
; __device__ __forceinline__ float sigmoid1702(float x) { return __builtin_amdgcn_rcpf(1.0f + __builtin_amdgcn_exp2f(x * (-1.702f * 1.4426950408889634f))); }
;     __device__ __forceinline__ void operator()(const f32x4 (&acc)[2][2][4][2], const Unit& u, int wr, int wc, int fr, int fq) const {
;     ...
;         for (int ai = 0; ai < 2; ++ai)
; #pragma unroll
;             for (int m = 0; m < 4; ++m) { f32x4 ga = acc[ai][0][m][0] * F8_DESCALE + g0, gb = acc[ai][0][m][1] * F8_DESCALE + g1, ua = acc[ai][1][m][0] * D4 + u0, ub = acc[ai][1][m][1] * D4 + u1;
; #pragma unroll
;                 for (int q = 0; q < 4; ++q) { float gg = fminf(ga[q], 7.0f), uu = __builtin_amdgcn_fmed3f(ua[q], -6.0f * F8_ASCALE, 8.0f * F8_ASCALE); ga[q] = uu * (gg * sigmoid1702(gg));
;                     gg = fminf(gb[q], 7.0f); uu = __builtin_amdgcn_fmed3f(ub[q], -6.0f * F8_ASCALE, 8.0f * F8_ASCALE); gb[q] = uu * (gg * sigmoid1702(gg)); }
;                 v2u w; w.x = pk4_fp8_nc(ga[0], ga[1], ga[2], ga[3]); w.y = pk4_fp8_nc(gb[0], gb[1], gb[2], gb[3]);
;                 *(v2u*)(ACT + (size_t)(row0 + ai * 128 + m * 16) * 2048 + col) = w; }
	v_add_f32_e32 v20, 1.0, v24
	v_min_f32_e32 v24, 0x40e00000, v32
	v_rcp_f32_e32 v20, v20
	v_mul_f32_e32 v28, 0xc01d265f, v24
	v_exp_f32_e32 v28, v28
	v_mul_f32_e32 v16, v18, v16
	v_fmamk_f32 v18, v56, 0x3b800000, v13
	v_med3_f32 v18, v18, s57, v194
	v_mul_f32_e32 v20, v22, v20
	v_min_f32_e32 v22, 0x40e00000, v29
	v_mul_f32_e32 v18, v18, v20
	v_add_f32_e32 v20, 1.0, v28
	v_mul_f32_e32 v28, 0xc01d265f, v22
	v_rcp_f32_e32 v20, v20
	v_exp_f32_e32 v28, v28
	v_fmamk_f32 v29, v48, 0x3b800000, v11
	v_med3_f32 v29, v29, s57, v194
	v_mul_f32_e32 v20, v24, v20
	v_add_f32_e32 v24, 1.0, v28
	v_rcp_f32_e32 v24, v24
	v_mul_f32_e32 v20, v29, v20
	v_fmamk_f32 v28, v57, 0x3b800000, v21
	v_med3_f32 v28, v28, s57, v194
	v_mul_f32_e32 v22, v22, v24
	v_min_f32_e32 v24, 0x40e00000, v33
	v_mul_f32_e32 v29, 0xc01d265f, v24
	v_exp_f32_e32 v29, v29
	v_mul_f32_e32 v22, v28, v22
	v_fmamk_f32 v28, v49, 0x3b800000, v23
	v_med3_f32 v30, v28, s57, v194
	v_add_f32_e32 v28, 1.0, v29
	v_rcp_f32_e32 v31, v28
	v_mov_b32_e32 v29, v167
	v_cvt_pk_fp8_f32 v29, v12, v16
	v_mov_b32_e32 v28, v167
	v_cvt_pk_fp8_f32 v28, v10, v14
	v_mul_f32_e32 v10, v24, v31
	v_pk_fma_f32 v[6:7], v[50:51], s[20:21], v[6:7] op_sel_hi:[1,0,1]
	v_mul_f32_e32 v10, v30, v10
	v_min_f32_e32 v6, 0x40e00000, v6
	v_cvt_pk_fp8_f32 v29, v20, v10 op_sel:[0,0,1]
	v_mul_f32_e32 v10, 0xc01d265f, v6
	v_exp_f32_e32 v10, v10
	v_pk_fma_f32 v[2:3], v[42:43], s[20:21], v[2:3] op_sel_hi:[1,0,1]
	v_min_f32_e32 v7, 0x40e00000, v7
	v_min_f32_e32 v2, 0x40e00000, v2
	v_add_f32_e32 v10, 1.0, v10
	v_mul_f32_e32 v12, 0xc01d265f, v2
	v_rcp_f32_e32 v10, v10
	v_exp_f32_e32 v12, v12
	v_min_f32_e32 v3, 0x40e00000, v3
	v_fmac_f32_e32 v25, 0x3b800000, v38
	v_mul_f32_e32 v6, v6, v10
	v_add_f32_e32 v10, 1.0, v12
	v_mul_f32_e32 v12, 0xc01d265f, v7
	v_rcp_f32_e32 v10, v10
	v_exp_f32_e32 v12, v12
	v_pk_fma_f32 v[8:9], v[52:53], s[20:21], v[8:9] op_sel_hi:[1,0,1]
	v_med3_f32 v14, v25, s57, v194
	v_mul_f32_e32 v2, v2, v10
	v_add_f32_e32 v10, 1.0, v12
	v_rcp_f32_e32 v10, v10
	v_fmac_f32_e32 v19, 0x3b800000, v34
	v_mul_f32_e32 v6, v14, v6
	v_med3_f32 v14, v19, s57, v194
	v_mul_f32_e32 v7, v7, v10
	v_mul_f32_e32 v10, 0xc01d265f, v3
	v_exp_f32_e32 v10, v10
	v_min_f32_e32 v8, 0x40e00000, v8
	v_mul_f32_e32 v12, v14, v2
	v_mul_f32_e32 v14, 0xc01d265f, v8
	v_add_f32_e32 v10, 1.0, v10
	v_rcp_f32_e32 v10, v10
	v_exp_f32_e32 v14, v14
	v_fmac_f32_e32 v17, 0x3b800000, v39
	v_med3_f32 v2, v17, s57, v194
	v_fmac_f32_e32 v15, 0x3b800000, v35
	v_pk_fma_f32 v[4:5], v[44:45], s[20:21], v[4:5] op_sel_hi:[1,0,1]
	v_mul_f32_e32 v7, v2, v7
	v_med3_f32 v2, v15, s57, v194
	v_mul_f32_e32 v3, v3, v10
	v_mul_f32_e32 v10, v2, v3
	v_add_f32_e32 v2, 1.0, v14
	v_min_f32_e32 v3, 0x40e00000, v4
	v_rcp_f32_e32 v2, v2
	v_mul_f32_e32 v4, 0xc01d265f, v3
	v_exp_f32_e32 v4, v4
	v_fmac_f32_e32 v13, 0x3b800000, v40
	v_med3_f32 v13, v13, s57, v194
	v_mul_f32_e32 v2, v8, v2
	v_mul_f32_e32 v8, v13, v2
	v_add_f32_e32 v2, 1.0, v4
	v_min_f32_e32 v4, 0x40e00000, v9
	v_mul_f32_e32 v9, 0xc01d265f, v4
	v_rcp_f32_e32 v2, v2
	v_exp_f32_e32 v9, v9
	v_fmac_f32_e32 v11, 0x3b800000, v36
	v_med3_f32 v11, v11, s57, v194
	v_mul_f32_e32 v2, v3, v2
	v_add_f32_e32 v3, 1.0, v9
	v_rcp_f32_e32 v3, v3
	v_fmac_f32_e32 v21, 0x3b800000, v41
	v_mul_f32_e32 v9, v11, v2
	v_med3_f32 v2, v21, s57, v194
	v_mul_f32_e32 v3, v4, v3
	v_min_f32_e32 v4, 0x40e00000, v5
	v_mul_f32_e32 v5, 0xc01d265f, v4
	v_exp_f32_e32 v5, v5
	v_mul_f32_e32 v11, v2, v3
	v_mov_b32_e32 v3, v167
	v_cvt_pk_fp8_f32 v3, v12, v10
	v_add_f32_e32 v2, 1.0, v5
	v_rcp_f32_e32 v5, v2
	v_mov_b32_e32 v2, v167
	v_cvt_pk_fp8_f32 v2, v6, v7
	v_fmac_f32_e32 v23, 0x3b800000, v37
	v_med3_f32 v13, v23, s57, v194
	v_mul_f32_e32 v4, v4, v5
	v_add_co_u32_e32 v30, vcc, s60, v26
	v_mul_f32_e32 v4, v13, v4
	v_cvt_pk_fp8_f32 v28, v18, v22 op_sel:[0,0,1]
	v_addc_co_u32_e32 v31, vcc, 0, v27, vcc
	v_cvt_pk_fp8_f32 v2, v8, v11 op_sel:[0,0,1]
	v_cvt_pk_fp8_f32 v3, v9, v4 op_sel:[0,0,1]
	v_add_co_u32_e32 v4, vcc, 0x58000, v26
	global_store_dwordx2 v[30:31], v[28:29], off
	s_nop 0
	v_addc_co_u32_e32 v5, vcc, 0, v27, vcc
	s_and_b64 vcc, exec, s[0:1]
	s_mov_b64 s[0:1], -1
	global_store_dwordx2 v[4:5], v[2:3], off
	s_cbranch_vccnz .LBB0_1408
	s_andn2_b64 vcc, exec, s[4:5]
	s_cbranch_vccnz .LBB0_1407
	s_barrier
	s_branch .LBB0_1407
